# helper share 12x171 runs (tuning)
# speedup vs baseline: 1.0040x; 1.0040x over previous
; #define LDS_AS __attribute__((address_space(3)))
; #define OPAQUE_TID(P) (((P).wid0 << 6) | lane_id_now())
; #define LAS __attribute__((address_space(3)))
; template <int NS, bool STREAM_ONLY = false>
; DI void convert_experts_dma(const Params& p, LDS_AS unsigned char* lds, int bid, int nb) {
;   const int tid = OPAQUE_TID(p), wid = __builtin_amdgcn_readfirstlane(tid >> 6), lane = tid & 63;
;   constexpr int NT = 32 * 1536;
;   const int nvalid = bid < NT / CVG ? CVG * ((NT / CVG - bid + nb - 1) / nb) : 0;
; __global__ void __launch_bounds__(NTHREADS, 2) k_forward(Params p_in) {
;     ...
;   if (is_cv) {
;     {
;       volatile LAS unsigned* stw = (volatile LAS unsigned*)dyn_smem;
;       const unsigned s0 = stw[0], s1 = stw[1];
;       __syncthreads();
;       convert_experts_dma<5>(p, (LDS_AS unsigned char*)dyn_smem, cvid, ncv);
.LBB0_1119:
	s_or_b64 exec, exec, s[0:1]
	s_mov_b64 s[12:13], 0
	s_mov_b32 s20, 0
	s_mov_b64 s[0:1], 0
	v_readlane_b32 s97, v255, 13
	s_mov_b32 s99, s96
	s_nop 0
	s_mov_b32 s98, s97
	s_cmp_lg_u32 s55, 0
	s_cbranch_scc0 .LBB0_1181
	v_readlane_b32 s98, v255, 17
	s_sub_i32 s99, s96, s55
	s_add_i32 s98, s98, 0x27fc
	s_branch .LBB0_1181
.LBB0_1121:
	v_mov_b32_e32 v0, 0
	ds_read_b32 v2, v0
	ds_read_b32 v3, v0 offset:4
	s_waitcnt lgkmcnt(0)
	s_barrier
	v_mbcnt_lo_u32_b32 v0, -1, 0
	v_mbcnt_hi_u32_b32 v0, -1, v0
	s_mov_b32 s6, 0
	v_or_b32_e32 v1, s87, v0
	s_cmpk_gt_i32 s54, 0x27fb
	v_readfirstlane_b32 s0, v1
	s_mov_b32 s18, 0
	s_cbranch_scc1 .LBB0_1123
	s_abs_i32 s1, s55
	v_cvt_f32_u32_e32 v1, s1
	s_sub_i32 s2, s55, s54
	s_add_i32 s3, s2, 0x27fb
	s_sub_i32 s2, 0xffffd805, s2
	v_rcp_iflag_f32_e32 v1, v1
	s_xor_b32 s5, s3, s55
	s_sub_i32 s4, 0, s1
	s_max_i32 s2, s3, s2
	v_mul_f32_e32 v1, 0x4f7ffffe, v1
	v_cvt_u32_f32_e32 v1, v1
	s_ashr_i32 s3, s5, 31
	v_readfirstlane_b32 s5, v1
	s_mul_i32 s4, s4, s5
	s_mul_hi_u32 s4, s5, s4
	s_add_i32 s5, s5, s4
	s_mul_hi_u32 s4, s2, s5
	s_mul_i32 s5, s4, s1
	s_sub_i32 s2, s2, s5
	s_add_i32 s7, s4, 1
	s_sub_i32 s5, s2, s1
	s_cmp_ge_u32 s2, s1
	s_cselect_b32 s4, s7, s4
	s_cselect_b32 s2, s5, s2
	s_add_i32 s5, s4, 1
	s_cmp_ge_u32 s2, s1
	s_cselect_b32 s1, s5, s4
	s_xor_b32 s1, s1, s3
	s_sub_i32 s1, s1, s3
	s_lshl_b32 s18, s1, 2
